# code placement scan: v045 + L0 in-proj K-loop shifted +4 bytes (MFMAs 8-byte aligned like the other bf16 loops)
# speedup vs baseline: 1.0113x; 1.0076x over previous
.LBB0_134:
	s_andn2_b64 vcc, exec, s[2:3]
	v_writelane_b32 v254, s52, 39
	s_cbranch_vccnz .LBB0_199
	v_ashrrev_i32_e32 v3, 31, v1
	v_lshrrev_b32_e32 v3, 26, v3
	v_add_u32_e32 v3, v1, v3
	v_ashrrev_i32_e32 v10, 6, v3
	v_bfe_i32 v3, v1, 27, 1
	v_lshlrev_b32_e32 v2, 4, v1
	v_lshrrev_b32_e32 v3, 22, v3
	v_add_u32_e32 v3, v2, v3
	v_and_b32_e32 v3, 0xfffffc00, v3
	v_sub_u32_e32 v3, v2, v3
	v_lshrrev_b32_e32 v4, 4, v3
	v_bitop3_b32 v4, v4, v3, 32 bitop3:0x6c
	v_ashrrev_i32_e32 v3, 31, v3
	v_lshrrev_b32_e32 v3, 26, v3
	v_add_u32_e32 v3, v4, v3
	v_ashrrev_i32_e32 v11, 6, v3
	v_lshlrev_b32_e32 v5, 3, v10
	v_mul_i32_i24_e32 v6, 64, v11
	v_and_b32_e32 v5, -16, v5
	v_sub_u32_e32 v4, v4, v6
	v_mov_b32_e32 v6, 1
	v_add_u32_e32 v3, v11, v5
	v_lshlrev_b32_e32 v5, 5, v10
	v_ashrrev_i16_sdwa v4, v6, sext(v4) dst_sel:DWORD dst_unused:UNUSED_PAD src0_sel:DWORD src1_sel:BYTE_0
	v_and_b32_e32 v5, 32, v5
	v_bfe_i32 v12, v4, 0, 16
	v_and_b32_e32 v8, 3, v11
	s_mov_b32 s2, 0x1fffe0
	v_add_lshl_u32 v5, v5, v12, 1
	v_add_u32_e32 v2, 0x2000, v2
	v_lshlrev_b32_e32 v4, 1, v3
	v_lshrrev_b32_e32 v7, 2, v3
	v_and_or_b32 v8, v3, s2, v8
	v_lshl_add_u32 v146, v3, 11, v5
	v_ashrrev_i32_e32 v3, 31, v2
	v_lshrrev_b32_e32 v3, 22, v3
	v_add_u32_e32 v3, v2, v3
	v_ashrrev_i32_e32 v13, 10, v3
	v_mul_i32_i24_e32 v3, 0x400, v13
	v_sub_u32_e32 v2, v2, v3
	v_and_b32_e32 v4, 24, v4
	v_and_b32_e32 v7, 4, v7
	v_lshrrev_b32_e32 v3, 4, v2
	v_or3_b32 v4, v8, v7, v4
	v_bitop3_b32 v2, v3, v2, 32 bitop3:0x6c
	s_add_u32 s22, s94, s6
	v_lshl_add_u32 v148, v4, 11, v5
	v_ashrrev_i32_e32 v4, 31, v2
	s_addc_u32 s23, s95, 0
	v_lshrrev_b32_e32 v4, 26, v4
	s_add_u32 s31, s22, 0xca00000
	v_add_u32_e32 v4, v2, v4
	s_addc_u32 s33, s23, 0
	v_lshlrev_b32_e32 v3, 3, v13
	v_ashrrev_i32_e32 v14, 6, v4
	v_and_b32_e32 v4, 0xc0, v4
	s_add_u32 s35, s22, 0x400000
	v_and_b32_e32 v3, -16, v3
	v_sub_u32_e32 v2, v2, v4
	s_addc_u32 s37, s23, 0
	s_ashr_i32 s9, s20, 6
	v_add_u32_e32 v3, v14, v3
	v_ashrrev_i16_sdwa v2, v6, sext(v2) dst_sel:DWORD dst_unused:UNUSED_PAD src0_sel:DWORD src1_sel:BYTE_0
	v_and_b32_e32 v6, 3, v14
	s_ashr_i32 s55, s54, 31
	s_ashr_i32 s5, s4, 31
	v_and_or_b32 v6, v3, s2, v6
	s_ashr_i32 s26, s20, 8
	s_lshl_b32 s48, s9, 10
	s_lshl_b64 s[2:3], s[54:55], 19
	s_lshl_b64 s[6:7], s[4:5], 19
	s_add_u32 s62, s35, s6
	v_lshlrev_b32_e32 v5, 5, v13
	v_bfe_i32 v15, v2, 0, 16
	v_lshlrev_b32_e32 v2, 1, v3
	v_lshrrev_b32_e32 v4, 2, v3
	s_addc_u32 s63, s37, s7
	s_add_i32 s49, s48, 0
	v_and_b32_e32 v5, 32, v5
	v_and_b32_e32 v2, 24, v2
	v_and_b32_e32 v4, 4, v4
	s_add_i32 m0, s49, 0x10000
	v_or3_b32 v2, v6, v4, v2
	v_add_lshl_u32 v4, v5, v15, 1
	global_load_lds_dwordx4 v148, s[62:63]
	s_add_i32 m0, s49, 0x12000
	v_lshl_add_u32 v152, v2, 11, v4
	s_add_u32 s6, s62, 0x40000
	global_load_lds_dwordx4 v152, s[62:63]
	s_addc_u32 s7, s63, 0
	s_add_i32 m0, s49, 0x14000
	v_lshl_add_u32 v150, v3, 11, v4
	global_load_lds_dwordx4 v148, s[6:7]
	s_add_i32 m0, s49, 0x16000
	s_add_u32 s2, s31, s2
	s_addc_u32 s3, s33, s3
	s_add_i32 s55, s49, 0x2000
	global_load_lds_dwordx4 v152, s[6:7]
	s_mov_b32 m0, s49
	s_add_u32 s6, s2, 0x40000
	global_load_lds_dwordx4 v146, s[2:3]
	s_mov_b32 m0, s55
	s_addc_u32 s7, s3, 0
	s_add_i32 s76, s49, 0x4000
	global_load_lds_dwordx4 v150, s[2:3]
	s_mov_b32 m0, s76
	s_add_i32 s77, s49, 0x6000
	global_load_lds_dwordx4 v146, s[6:7]
	s_mov_b32 m0, s77
	v_mov_b32_e32 v149, 0
	global_load_lds_dwordx4 v150, s[6:7]
	v_mov_b32_e32 v153, v149
	v_mov_b32_e32 v147, v149
	v_mov_b32_e32 v151, v149
	s_cmp_eq_u32 s26, 1
	s_mov_b32 s79, 0
	v_lshl_add_u64 v[8:9], s[62:63], 0, v[148:149]
	v_lshl_add_u64 v[6:7], s[62:63], 0, v[152:153]
	v_lshl_add_u64 v[2:3], s[2:3], 0, v[146:147]
	s_cselect_b64 s[6:7], -1, 0
	s_cmp_lg_u32 s26, 1
	v_lshl_add_u64 v[4:5], s[2:3], 0, v[150:151]
	s_cbranch_scc1 .LBB0_137
	s_barrier
	s_nop 0

.LBB0_258:
	s_or_b64 exec, exec, s[0:1]
	s_add_u32 s22, s94, s41
	s_addc_u32 s23, s95, 0
	s_add_u32 s10, s22, 0x10a00000
	s_addc_u32 s11, s23, 0
	s_and_b32 s48, s8, 31
	s_ashr_i32 s4, s8, 7
	s_xor_b32 s49, s48, 63
	s_lshl_b32 s0, s7, 8
	s_add_u32 s1, s22, s0
	s_addc_u32 s2, s23, 0
	s_add_u32 s52, s1, 0x10a00400
	s_addc_u32 s53, s2, 0
	s_add_u32 s54, s1, 0x10a00800
	s_addc_u32 s55, s2, 0
	s_add_u32 s62, s1, 0x10a00c00
	s_addc_u32 s63, s2, 0
	s_lshl_b32 s1, s7, 9
	s_add_u32 s1, s22, s1
	v_mov_b32_e32 v1, 0x3e4ccccd
	s_addc_u32 s2, s23, 0
	v_add_f32_e32 v214, s6, v1
	s_add_u32 s6, s1, 0x19a00000
	s_addc_u32 s7, s2, 0
	s_ashr_i32 s5, s4, 31
	s_lshl_b64 s[8:9], s[4:5], 14
	s_add_u32 s24, s10, s0
	s_mov_b32 s21, 0
	v_mov_b32_e32 v215, v214
	s_addc_u32 s25, s11, 0
	s_movk_i32 s5, 0x1200
	v_mov_b32_e32 v3, 0
	s_mov_b64 s[26:27], 0x48000
	s_mov_b64 s[28:29], 0x90000
	s_add_i32 s40, 0, 0x1e800
	s_mov_b64 s[30:31], 0xd8000
	s_mov_b32 s79, 0x41000000
	s_mov_b32 s80, 0xffff0000
	v_mov_b32_e32 v1, 0x3727c5ac
	v_mov_b32_e32 v226, 0x260
	s_movk_i32 s81, 0x7fff
	v_mov_b32_e32 v227, 0xff800000
	v_bfrev_b32_e32 v228, 0.5
	s_waitcnt lgkmcnt(0)
	s_barrier
	s_branch .LBB0_260
.LBB0_259:
	s_add_i32 s21, s21, 1
	s_cmp_eq_u32 s21, 4
	s_cbranch_scc1 .LBB0_349
	s_nop 0
	s_nop 0
	s_nop 0
	s_nop 0
	s_nop 0
	s_nop 0
	s_nop 0
	s_nop 0
	s_nop 0
	s_nop 0
	s_nop 0
	s_nop 0
	s_nop 0
	s_nop 0
	s_nop 0
.LBB0_260:
	s_lshr_b32 s84, s21, 1
	s_bitcmp0_b32 s21, 0
	s_cselect_b32 s82, s49, s48
	s_lshl_b32 s0, s84, 7
	s_add_u32 s3, s52, s0
	s_addc_u32 s33, s53, 0
	s_add_u32 s39, s54, s0
	v_mov_b32_e32 v36, v0
	s_mov_b32 s38, s82
	s_mov_b32 s0, s4
	s_addc_u32 s43, s55, 0
	s_ashr_i32 s1, s0, 31
	v_readfirstlane_b32 s2, v36
	s_lshl_b64 s[34:35], s[0:1], 14
	s_lshl_b32 s1, s38, 8
	s_ashr_i32 s83, s2, 6
	s_ashr_i32 s36, s1, 31
	s_add_u32 s34, s34, s1
	s_addc_u32 s35, s35, s36
	s_lshl_b32 s46, s83, 5
	s_ashr_i32 s36, s46, 31
	s_add_u32 s34, s34, s46
	s_addc_u32 s35, s35, s36
	s_mul_i32 s36, s35, 0x1200
	s_mul_hi_u32 s37, s34, 0x1200
	s_add_i32 s37, s37, s36
	s_mul_i32 s36, s34, 0x1200
	s_add_u32 s36, s3, s36
	s_addc_u32 s37, s33, s37
	s_mul_hi_i32 s3, s0, 0x4800000
	s_mul_i32 s0, s0, 0x4800000
	v_and_b32_e32 v230, 63, v36
	s_add_u32 s42, s39, s0
	s_addc_u32 s43, s43, s3
	v_mul_u32_u24_e32 v2, 0x900, v230
	s_add_u32 s44, s62, s0
	v_lshlrev_b32_e32 v2, 1, v2
	s_addc_u32 s45, s63, s3
	v_lshl_add_u64 v[4:5], s[42:43], 0, v[2:3]
	s_lshl_b32 s42, s83, 3
	s_lshl_b32 s0, s83, 4
	v_bfe_u32 v2, v36, 2, 4
	s_ashr_i32 s43, s42, 31
	v_and_or_b32 v2, s0, 48, v2
	s_ashr_i32 s0, s2, 3
	v_lshl_add_u64 v[216:217], s[42:43], 1, v[4:5]
	s_and_b32 s42, s0, 0xffffffe0
	v_mul_u32_u24_e32 v2, 0x900, v2
	s_ashr_i32 s43, s42, 31
	s_lshl_b32 s0, s83, 10
	v_lshlrev_b32_e32 v2, 1, v2
	v_lshlrev_b32_e32 v232, 3, v36
	s_cmp_lg_u32 0, -1
	v_lshl_add_u64 v[4:5], s[44:45], 0, v[2:3]
	v_and_b32_e32 v233, 24, v232
	s_cselect_b32 s3, 0, 0
	v_and_b32_e32 v231, 31, v36
	v_lshl_add_u64 v[4:5], s[42:43], 1, v[4:5]
	v_lshlrev_b32_e32 v2, 1, v233
	s_add_i32 s76, s0, s3
	s_mov_b32 m0, s76
	s_nop 0
	global_load_lds_dwordx4 v[216:217], off
	v_lshl_add_u64 v[218:219], v[4:5], 0, v[2:3]
	s_add_i32 s77, s76, 0x6000
	s_mov_b32 m0, s77
	s_nop 0
	global_load_lds_dwordx4 v[218:219], off
	s_mov_b64 s[42:43], 0x80
	v_mul_u32_u24_e32 v2, 0x900, v231
	v_bfe_u32 v229, v36, 5, 1
	v_lshl_add_u64 v[220:221], v[218:219], 0, s[42:43]
	s_add_i32 s3, s76, 0x8000
	s_mov_b32 m0, s3
	s_nop 0
	global_load_lds_dwordx4 v[220:221], off
	v_lshlrev_b32_e32 v2, 1, v2
	v_lshl_add_u64 v[4:5], v[216:217], 0, s[26:27]
	s_add_i32 s3, s76, 0x2000
	s_mov_b32 m0, s3
	s_nop 0
	global_load_lds_dwordx4 v[4:5], off
	v_lshl_or_b32 v2, v229, 4, v2
	global_load_dwordx4 v[154:157], v2, s[36:37]
	global_load_dwordx4 v[150:153], v2, s[36:37] offset:32
	global_load_dwordx4 v[146:149], v2, s[36:37] offset:64
	global_load_dwordx4 v[142:145], v2, s[36:37] offset:96
	s_mov_b64 s[36:37], 0x48080
	v_lshlrev_b32_e32 v2, 10, v229
	v_lshlrev_b32_e32 v4, 4, v231
	v_add3_u32 v240, 0, v2, v4
	v_lshl_add_u64 v[4:5], v[216:217], 0, s[28:29]
	s_add_i32 s3, s76, 0x4000
	v_lshl_add_u64 v[8:9], v[218:219], 0, s[36:37]
	s_mov_b32 m0, s3
	s_nop 0
	global_load_lds_dwordx4 v[4:5], off
	s_add_i32 s33, s76, 0xa000
	v_lshl_add_u64 v[6:7], v[218:219], 0, s[26:27]
	s_mov_b32 m0, s33
	s_nop 0
	global_load_lds_dwordx4 v[6:7], off
	s_add_i32 s39, s76, 0xc000
	s_mov_b32 m0, s39
	s_nop 0
	global_load_lds_dwordx4 v[8:9], off
	s_waitcnt vmcnt(6) lgkmcnt(0)
	s_barrier
	ds_read_b128 v[4:7], v240
	ds_read_b128 v[8:11], v240 offset:512
	ds_read_b128 v[38:41], v240 offset:2048
	ds_read_b128 v[42:45], v240 offset:2560
	s_add_i32 s3, s1, 0x100
	s_ashr_i32 s85, s3, 6
	v_lshlrev_b32_e32 v239, 2, v229
	v_or_b32_e32 v238, s46, v231
	s_cmp_gt_i32 s85, 4
	s_waitcnt vmcnt(3) lgkmcnt(3)
	v_mfma_f32_32x32x16_bf16 v[20:35], v[4:7], v[154:157], 0
	s_waitcnt lgkmcnt(2)
	v_mfma_f32_32x32x16_bf16 v[4:19], v[8:11], v[154:157], 0
	s_waitcnt vmcnt(2) lgkmcnt(1)
	v_mfma_f32_32x32x16_bf16 v[20:35], v[38:41], v[150:153], v[20:35]
	s_waitcnt lgkmcnt(0)
	v_mfma_f32_32x32x16_bf16 v[4:19], v[42:45], v[150:153], v[4:19]
	ds_read_b128 v[38:41], v240 offset:4096
	ds_read_b128 v[42:45], v240 offset:4608
	s_waitcnt vmcnt(1) lgkmcnt(1)
	v_mfma_f32_32x32x16_bf16 v[20:35], v[38:41], v[146:149], v[20:35]
	s_waitcnt lgkmcnt(0)
	v_mfma_f32_32x32x16_bf16 v[4:19], v[42:45], v[146:149], v[4:19]
	ds_read_b128 v[38:41], v240 offset:6144
	ds_read_b128 v[42:45], v240 offset:6656
	s_waitcnt vmcnt(0) lgkmcnt(1)
	v_mfma_f32_32x32x16_bf16 v[20:35], v[38:41], v[142:145], v[20:35]
	s_waitcnt lgkmcnt(0)
	v_mfma_f32_32x32x16_bf16 v[4:19], v[42:45], v[142:145], v[4:19]
	s_nop 15
	s_nop 7
	s_cbranch_scc1 .LBB0_262
	v_subrev_u32_e32 v2, s1, v239
	v_or_b32_e32 v37, 32, v2
	v_cmp_le_i32_e32 vcc, v37, v238
	v_or_b32_e32 v37, 33, v2
	s_nop 6
	v_cndmask_b32_e32 v4, v227, v4, vcc
	v_cmp_lt_i32_e32 vcc, v2, v238
	s_nop 1
	v_cndmask_b32_e32 v21, v227, v21, vcc
	v_cmp_le_i32_e32 vcc, v2, v238
	s_nop 1
	v_cndmask_b32_e32 v20, v227, v20, vcc
	v_cmp_le_i32_e32 vcc, v37, v238
	v_or_b32_e32 v37, 2, v2
	s_nop 0
	v_cndmask_b32_e32 v5, v227, v5, vcc
	v_cmp_le_i32_e32 vcc, v37, v238
	v_or_b32_e32 v37, 34, v2
	s_nop 0
	v_cndmask_b32_e32 v22, v227, v22, vcc
	v_cmp_le_i32_e32 vcc, v37, v238
	v_or_b32_e32 v37, 3, v2
	s_nop 0
	v_cndmask_b32_e32 v6, v227, v6, vcc
	v_cmp_le_i32_e32 vcc, v37, v238
	v_or_b32_e32 v37, 35, v2
	s_nop 0
	v_cndmask_b32_e32 v23, v227, v23, vcc
	v_cmp_le_i32_e32 vcc, v37, v238
	v_or_b32_e32 v37, 8, v2
	s_nop 0
	v_cndmask_b32_e32 v7, v227, v7, vcc
	v_cmp_le_i32_e32 vcc, v37, v238
	v_or_b32_e32 v37, 40, v2
	s_nop 0
	v_cndmask_b32_e32 v24, v227, v24, vcc
	v_cmp_le_i32_e32 vcc, v37, v238
	v_or_b32_e32 v37, 9, v2
	s_nop 0
	v_cndmask_b32_e32 v8, v227, v8, vcc
	v_cmp_le_i32_e32 vcc, v37, v238
	v_or_b32_e32 v37, 41, v2
	s_nop 0
	v_cndmask_b32_e32 v25, v227, v25, vcc
	v_cmp_le_i32_e32 vcc, v37, v238
	v_or_b32_e32 v37, 10, v2
	s_nop 0
	v_cndmask_b32_e32 v9, v227, v9, vcc
	v_cmp_le_i32_e32 vcc, v37, v238
	v_or_b32_e32 v37, 42, v2
	s_nop 0
	v_cndmask_b32_e32 v26, v227, v26, vcc
	v_cmp_le_i32_e32 vcc, v37, v238
	v_or_b32_e32 v37, 11, v2
	s_nop 0
	v_cndmask_b32_e32 v10, v227, v10, vcc
	v_cmp_le_i32_e32 vcc, v37, v238
	v_or_b32_e32 v37, 43, v2
	s_nop 0
	v_cndmask_b32_e32 v27, v227, v27, vcc
	v_cmp_le_i32_e32 vcc, v37, v238
	v_or_b32_e32 v37, 16, v2
	s_nop 0
	v_cndmask_b32_e32 v11, v227, v11, vcc
	v_cmp_le_i32_e32 vcc, v37, v238
	v_or_b32_e32 v37, 48, v2
	s_nop 0
	v_cndmask_b32_e32 v28, v227, v28, vcc
	v_cmp_le_i32_e32 vcc, v37, v238
	v_or_b32_e32 v37, 17, v2
	s_nop 0
	v_cndmask_b32_e32 v12, v227, v12, vcc
	v_cmp_le_i32_e32 vcc, v37, v238
	v_or_b32_e32 v37, 49, v2
	s_nop 0
	v_cndmask_b32_e32 v29, v227, v29, vcc
	v_cmp_le_i32_e32 vcc, v37, v238
	v_or_b32_e32 v37, 18, v2
	s_nop 0
	v_cndmask_b32_e32 v13, v227, v13, vcc
	v_cmp_le_i32_e32 vcc, v37, v238
	v_or_b32_e32 v37, 50, v2
	s_nop 0
	v_cndmask_b32_e32 v30, v227, v30, vcc
	v_cmp_le_i32_e32 vcc, v37, v238
	v_or_b32_e32 v37, 19, v2
	s_nop 0
	v_cndmask_b32_e32 v14, v227, v14, vcc
	v_cmp_le_i32_e32 vcc, v37, v238
	v_or_b32_e32 v37, 51, v2
	s_nop 0
	v_cndmask_b32_e32 v31, v227, v31, vcc
	v_cmp_le_i32_e32 vcc, v37, v238
	v_or_b32_e32 v37, 24, v2
	s_nop 0
	v_cndmask_b32_e32 v15, v227, v15, vcc
	v_cmp_le_i32_e32 vcc, v37, v238
	v_or_b32_e32 v37, 56, v2
	s_nop 0
	v_cndmask_b32_e32 v32, v227, v32, vcc
	v_cmp_le_i32_e32 vcc, v37, v238
	v_or_b32_e32 v37, 25, v2
	s_nop 0
	v_cndmask_b32_e32 v16, v227, v16, vcc
	v_cmp_le_i32_e32 vcc, v37, v238
	v_or_b32_e32 v37, 57, v2
	s_nop 0
	v_cndmask_b32_e32 v33, v227, v33, vcc
	v_cmp_le_i32_e32 vcc, v37, v238
	v_or_b32_e32 v37, 26, v2
	s_nop 0
	v_cndmask_b32_e32 v17, v227, v17, vcc
	v_cmp_le_i32_e32 vcc, v37, v238
	v_or_b32_e32 v37, 58, v2
	s_nop 0
	v_cndmask_b32_e32 v34, v227, v34, vcc
	v_cmp_le_i32_e32 vcc, v37, v238
	v_or_b32_e32 v37, 27, v2
	v_or_b32_e32 v2, 59, v2
	v_cndmask_b32_e32 v18, v227, v18, vcc
	v_cmp_le_i32_e32 vcc, v37, v238
	s_nop 1
	v_cndmask_b32_e32 v35, v227, v35, vcc
	v_cmp_le_i32_e32 vcc, v2, v238
	s_nop 1
	v_cndmask_b32_e32 v19, v227, v19, vcc
